# GEMM prologue de-serialisation: K-tile 1 stage DMAs issued together with K-tile 0's (first wait vmcnt(2)+barrier moved after them as vmcnt(8))
# baseline (speedup 1.0000x reference)
.LBB0_114:
	v_readlane_b32 s8, v251, 55
	v_mov_b32_e32 v139, v3
	v_readlane_b32 s9, v251, 56
	v_mov_b32_e32 v137, v3
	s_add_i32 m0, s42, 0x18000
	v_lshl_add_u64 v[6:7], s[8:9], 0, v[138:139]
	global_load_lds_dwordx4 v[6:7], off
	v_lshl_add_u64 v[6:7], s[8:9], 0, v[136:137]
	v_readlane_b32 s8, v251, 57
	s_add_i32 m0, s42, 0x1a000
	v_readlane_b32 s9, v251, 58
	s_add_i32 s51, s42, 0x8000
	v_mov_b32_e32 v143, v3
	global_load_lds_dwordx4 v[6:7], off
	v_lshl_add_u64 v[6:7], s[8:9], 0, v[2:3]
	s_mov_b32 m0, s51
	s_add_i32 s52, s42, 0xa000
	global_load_lds_dwordx4 v[6:7], off
	v_lshl_add_u64 v[6:7], s[8:9], 0, v[142:143]
	v_readlane_b32 s8, v251, 61
	s_mov_b32 m0, s52
	v_readlane_b32 s9, v251, 62
	global_load_lds_dwordx4 v[6:7], off
	s_add_i32 m0, s42, 0x1c000
	v_lshl_add_u64 v[6:7], s[8:9], 0, v[138:139]
	global_load_lds_dwordx4 v[6:7], off
	v_lshl_add_u64 v[6:7], s[8:9], 0, v[136:137]
	s_add_i32 m0, s42, 0x1e000
	v_and_b32_e32 v5, 15, v4
	global_load_lds_dwordx4 v[6:7], off
	s_waitcnt vmcnt(8)
	s_barrier
	v_lshrrev_b32_e32 v6, 1, v4
	v_and_b32_e32 v6, 24, v6
	v_lshlrev_b32_e32 v7, 1, v6
	v_lshlrev_b32_e32 v4, 2, v4
	v_lshl_or_b32 v159, s6, 6, v5
	v_lshl_or_b32 v5, v5, 6, v7
	s_lshl_b32 s6, s6, 13
	v_and_b32_e32 v4, 32, v4
	s_lshl_b32 s5, s5, 5
	v_bitop3_b32 v7, v5, s6, v4 bitop3:0xde
	s_and_b32 s6, s5, 0x60
	s_lshl_b32 s5, s6, 7
	v_bitop3_b32 v160, v5, s5, v4 bitop3:0xde
	s_waitcnt vmcnt(6)
	s_cmpk_lt_u32 s4, 0x100
	v_or_b32_e32 v4, s6, v6
	v_add_u32_e32 v5, 0, v160
	v_readlane_b32 s6, v251, 51
	v_readlane_b32 s12, v251, 59
	s_cselect_b64 s[4:5], -1, 0
	s_mov_b32 s53, 0
	v_add_u32_e32 v161, 0x10000, v5
	v_add_u32_e32 v162, 0x14000, v5
	v_add_u32_e32 v163, 0, v7
	v_lshlrev_b32_e32 v146, 1, v4
	s_mov_b32 s55, s6
	v_readlane_b32 s56, v251, 49
	v_readlane_b32 s13, v251, 60
	s_barrier
	v_readlane_b32 s7, v251, 52
	s_waitcnt vmcnt(0)
	s_branch .LBB0_117

.LBB0_133:
	s_lshl_b32 s6, s6, 5
	s_and_b32 s9, s6, 0x60
	s_lshl_b32 s8, s3, 13
	s_lshl_b32 s10, s9, 7
	s_add_u32 s6, s14, 0x8000
	v_mov_b32_e32 v211, v3
	s_addc_u32 s7, s15, 0
	v_mov_b32_e32 v209, v3
	s_add_i32 m0, s47, 0x18000
	v_lshl_add_u64 v[6:7], s[6:7], 0, v[210:211]
	global_load_lds_dwordx4 v[6:7], off
	v_lshl_add_u64 v[6:7], s[6:7], 0, v[208:209]
	v_readlane_b32 s6, v251, 57
	s_add_i32 m0, s47, 0x1a000
	v_readlane_b32 s7, v251, 58
	s_add_i32 s55, s47, 0x8000
	v_mov_b32_e32 v215, v3
	global_load_lds_dwordx4 v[6:7], off
	v_lshl_add_u64 v[6:7], s[6:7], 0, v[2:3]
	s_mov_b32 m0, s55
	s_add_i32 s56, s47, 0xa000
	global_load_lds_dwordx4 v[6:7], off
	v_lshl_add_u64 v[6:7], s[6:7], 0, v[214:215]
	s_add_u32 s6, s14, 0xc000
	s_mov_b32 m0, s56
	s_addc_u32 s7, s15, 0
	global_load_lds_dwordx4 v[6:7], off
	s_add_i32 m0, s47, 0x1c000
	v_lshl_add_u64 v[6:7], s[6:7], 0, v[210:211]
	global_load_lds_dwordx4 v[6:7], off
	v_lshl_add_u64 v[6:7], s[6:7], 0, v[208:209]
	s_add_i32 m0, s47, 0x1e000
	v_and_b32_e32 v5, 15, v4
	global_load_lds_dwordx4 v[6:7], off
	s_waitcnt vmcnt(8)
	s_barrier
	v_lshrrev_b32_e32 v6, 1, v4
	v_and_b32_e32 v6, 24, v6
	v_lshlrev_b32_e32 v7, 1, v6
	v_lshlrev_b32_e32 v4, 2, v4
	v_lshl_or_b32 v242, s3, 6, v5
	v_lshl_or_b32 v5, v5, 6, v7
	v_and_b32_e32 v4, 32, v4
	v_bitop3_b32 v7, v5, s8, v4 bitop3:0xde
	v_bitop3_b32 v243, v5, s10, v4 bitop3:0xde
	s_cmpk_lt_u32 s2, 0x100
	v_or_b32_e32 v4, s9, v6
	v_readlane_b32 s2, v251, 63
	s_waitcnt vmcnt(6)
	v_lshlrev_b32_e32 v4, 1, v4
	v_mov_b32_e32 v5, v3
	v_readlane_b32 s3, v252, 0
	s_cselect_b64 s[6:7], -1, 0
	s_mov_b32 s57, 0
	v_lshl_add_u64 v[218:219], s[2:3], 0, v[4:5]
	v_readlane_b32 s2, v254, 29
	v_add_u32_e32 v244, 0, v7
	s_mov_b32 s12, s2
	v_readlane_b32 s59, v254, 35
	s_barrier
	s_branch .LBB0_136

.LBB0_283:
	s_lshl_b32 s6, s6, 5
	s_and_b32 s9, s6, 0x60
	s_lshl_b32 s8, s3, 13
	s_lshl_b32 s10, s9, 7
	s_add_u32 s6, s14, 0x8000
	v_mov_b32_e32 v211, v3
	s_addc_u32 s7, s15, 0
	v_mov_b32_e32 v209, v3
	s_add_i32 m0, s45, 0x18000
	v_lshl_add_u64 v[6:7], s[6:7], 0, v[210:211]
	global_load_lds_dwordx4 v[6:7], off
	v_lshl_add_u64 v[6:7], s[6:7], 0, v[208:209]
	v_readlane_b32 s6, v253, 24
	s_add_i32 m0, s45, 0x1a000
	v_readlane_b32 s7, v253, 25
	s_add_i32 s54, s45, 0x8000
	v_mov_b32_e32 v215, v3
	global_load_lds_dwordx4 v[6:7], off
	v_lshl_add_u64 v[6:7], s[6:7], 0, v[2:3]
	s_mov_b32 m0, s54
	s_add_i32 s55, s45, 0xa000
	global_load_lds_dwordx4 v[6:7], off
	v_lshl_add_u64 v[6:7], s[6:7], 0, v[214:215]
	s_add_u32 s6, s14, 0xc000
	s_mov_b32 m0, s55
	s_addc_u32 s7, s15, 0
	global_load_lds_dwordx4 v[6:7], off
	s_add_i32 m0, s45, 0x1c000
	v_lshl_add_u64 v[6:7], s[6:7], 0, v[210:211]
	global_load_lds_dwordx4 v[6:7], off
	v_lshl_add_u64 v[6:7], s[6:7], 0, v[208:209]
	s_add_i32 m0, s45, 0x1e000
	v_and_b32_e32 v5, 15, v4
	global_load_lds_dwordx4 v[6:7], off
	s_waitcnt vmcnt(8)
	s_barrier
	v_lshrrev_b32_e32 v6, 1, v4
	v_and_b32_e32 v6, 24, v6
	v_lshlrev_b32_e32 v7, 1, v6
	v_lshlrev_b32_e32 v4, 2, v4
	v_lshl_or_b32 v242, s3, 6, v5
	v_lshl_or_b32 v5, v5, 6, v7
	v_and_b32_e32 v4, 32, v4
	v_bitop3_b32 v7, v5, s8, v4 bitop3:0xde
	v_bitop3_b32 v243, v5, s10, v4 bitop3:0xde
	s_waitcnt vmcnt(6)
	v_or_b32_e32 v4, s9, v6
	s_cmpk_lt_u32 s2, 0x100
	v_lshlrev_b32_e32 v4, 1, v4
	v_mov_b32_e32 v5, v3
	v_readlane_b32 s2, v254, 29
	s_cselect_b64 s[6:7], -1, 0
	v_lshl_add_u64 v[218:219], s[78:79], 0, v[4:5]
	s_mov_b32 s56, 0
	v_add_u32_e32 v244, 0, v7
	s_mov_b32 s12, s2
	v_readlane_b32 s58, v254, 35
	s_barrier
	s_branch .LBB0_286

.LBB0_487:
	s_and_b64 s[2:3], s[2:3], exec
	v_readlane_b32 s2, v253, 28
	s_cselect_b32 s52, s20, s2
	s_lshl_b32 s2, s8, 5
	s_and_b32 s8, s2, 0x60
	s_lshl_b32 s9, s7, 13
	s_lshl_b32 s10, s8, 7
	s_add_u32 s2, s12, 0x8000
	v_mov_b32_e32 v211, v3
	s_addc_u32 s3, s13, 0
	v_mov_b32_e32 v209, v3
	s_add_i32 m0, s43, 0x18000
	v_lshl_add_u64 v[6:7], s[2:3], 0, v[210:211]
	global_load_lds_dwordx4 v[6:7], off
	v_lshl_add_u64 v[6:7], s[2:3], 0, v[208:209]
	v_readlane_b32 s2, v251, 57
	s_add_i32 m0, s43, 0x1a000
	v_readlane_b32 s3, v251, 58
	s_add_i32 s53, s43, 0x8000
	v_mov_b32_e32 v215, v3
	global_load_lds_dwordx4 v[6:7], off
	v_lshl_add_u64 v[6:7], s[2:3], 0, v[2:3]
	s_mov_b32 m0, s53
	s_add_i32 s54, s43, 0xa000
	global_load_lds_dwordx4 v[6:7], off
	v_lshl_add_u64 v[6:7], s[2:3], 0, v[214:215]
	s_add_u32 s2, s12, 0xc000
	s_mov_b32 m0, s54
	s_addc_u32 s3, s13, 0
	global_load_lds_dwordx4 v[6:7], off
	s_add_i32 m0, s43, 0x1c000
	v_lshl_add_u64 v[6:7], s[2:3], 0, v[210:211]
	global_load_lds_dwordx4 v[6:7], off
	v_lshl_add_u64 v[6:7], s[2:3], 0, v[208:209]
	s_add_i32 m0, s43, 0x1e000
	v_and_b32_e32 v5, 15, v4
	global_load_lds_dwordx4 v[6:7], off
	s_waitcnt vmcnt(8)
	s_barrier
	v_lshrrev_b32_e32 v6, 1, v4
	v_and_b32_e32 v6, 24, v6
	v_lshlrev_b32_e32 v7, 1, v6
	v_lshlrev_b32_e32 v4, 2, v4
	v_lshl_or_b32 v240, s7, 6, v5
	v_lshl_or_b32 v5, v5, 6, v7
	v_and_b32_e32 v4, 32, v4
	s_waitcnt vmcnt(6)
	v_bitop3_b32 v7, v5, s9, v4 bitop3:0xde
	s_cmpk_lt_u32 s6, 0x100
	v_bitop3_b32 v241, v5, s10, v4 bitop3:0xde
	s_cselect_b64 s[6:7], -1, 0
	s_ashr_i32 s55, s52, 31
	v_or_b32_e32 v242, s8, v6
	s_mov_b32 s56, 0
	v_add_u32_e32 v243, 0, v7
	v_readlane_b32 s58, v254, 32
	v_readlane_b32 s59, v254, 37
	s_barrier
	s_branch .LBB0_490

.LBB0_1151:
	v_bfe_u32 v5, v4, 4, 2
	v_lshrrev_b32_e32 v6, 4, v4
	v_and_b32_e32 v219, 15, v4
	v_lshlrev_b32_e32 v7, 3, v5
	v_lshlrev_b32_e32 v5, 4, v5
	v_lshlrev_b32_e32 v4, 2, v4
	s_and_b32 s38, s4, 3
	v_lshl_or_b32 v5, v219, 6, v5
	s_lshl_b32 s2, s5, 13
	v_and_b32_e32 v4, 32, v4
	s_lshl_b32 s68, s5, 6
	v_bitop3_b32 v8, v5, s2, v4 bitop3:0xde
	s_lshl_b32 s2, s38, 12
	v_bitop3_b32 v9, v5, s2, v4 bitop3:0xde
	s_add_u32 s2, s14, 0x8000
	v_mov_b32_e32 v209, v3
	s_addc_u32 s3, s15, 0
	s_add_i32 s69, s9, 0x18000
	v_mov_b32_e32 v211, v3
	v_lshl_add_u64 v[4:5], s[2:3], 0, v[208:209]
	s_mov_b32 m0, s69
	global_load_lds_dwordx4 v[4:5], off
	v_lshl_add_u64 v[4:5], s[2:3], 0, v[210:211]
	s_add_i32 s70, s9, 0x1a000
	v_readlane_b32 s2, v254, 21
	s_mov_b32 m0, s70
	v_readlane_b32 s3, v254, 22
	s_add_i32 s71, s9, 0x8000
	v_mov_b32_e32 v213, v3
	global_load_lds_dwordx4 v[4:5], off
	v_lshl_add_u64 v[4:5], s[2:3], 0, v[2:3]
	s_mov_b32 m0, s71
	s_add_i32 s72, s9, 0xa000
	global_load_lds_dwordx4 v[4:5], off
	v_lshl_add_u64 v[4:5], s[2:3], 0, v[212:213]
	s_add_u32 s2, s14, 0xc000
	s_mov_b32 m0, s72
	s_addc_u32 s3, s15, 0
	s_add_i32 s73, s9, 0x1c000
	global_load_lds_dwordx4 v[4:5], off
	v_lshl_add_u64 v[4:5], s[2:3], 0, v[208:209]
	s_mov_b32 m0, s73
	s_add_i32 s74, s9, 0x1e000
	global_load_lds_dwordx4 v[4:5], off
	v_lshl_add_u64 v[4:5], s[2:3], 0, v[210:211]
	s_mov_b32 m0, s74
	v_lshl_or_b32 v221, s38, 5, v7
	global_load_lds_dwordx4 v[4:5], off
	s_waitcnt vmcnt(8)
	s_barrier
	s_waitcnt vmcnt(6)
	v_bitop3_b32 v222, s4, v6, 3 bitop3:0xa8
	v_mov_b32_e32 v6, v3
	v_mov_b32_e32 v7, v3
	s_cmpk_lt_u32 s11, 0x100
	v_mov_b32_e32 v4, v3
	v_mov_b32_e32 v5, v3
	v_mov_b32_e32 v68, 0
	v_add_u32_e32 v224, 0, v9
	v_add_u32_e32 v225, 0, v8
	v_mov_b64_e32 v[10:11], v[6:7]
	v_mov_b64_e32 v[14:15], v[6:7]
	v_mov_b64_e32 v[18:19], v[6:7]
	v_mov_b64_e32 v[22:23], v[6:7]
	v_mov_b64_e32 v[26:27], v[6:7]
	v_mov_b64_e32 v[30:31], v[6:7]
	v_mov_b64_e32 v[34:35], v[6:7]
	v_mov_b64_e32 v[38:39], v[6:7]
	v_mov_b64_e32 v[42:43], v[6:7]
	v_mov_b64_e32 v[46:47], v[6:7]
	v_mov_b64_e32 v[50:51], v[6:7]
	v_mov_b64_e32 v[54:55], v[6:7]
	v_mov_b64_e32 v[58:59], v[6:7]
	v_mov_b64_e32 v[62:63], v[6:7]
	v_mov_b64_e32 v[66:67], v[6:7]
	s_cselect_b64 s[38:39], -1, 0
	v_or_b32_e32 v223, s5, v222
	s_mov_b32 s75, 0
	v_mov_b64_e32 v[8:9], v[4:5]
	v_mov_b64_e32 v[12:13], v[4:5]
	v_mov_b64_e32 v[16:17], v[4:5]
	v_mov_b64_e32 v[20:21], v[4:5]
	v_mov_b64_e32 v[24:25], v[4:5]
	v_mov_b64_e32 v[28:29], v[4:5]
	v_mov_b64_e32 v[32:33], v[4:5]
	v_mov_b64_e32 v[36:37], v[4:5]
	v_mov_b64_e32 v[40:41], v[4:5]
	v_mov_b64_e32 v[44:45], v[4:5]
	v_mov_b64_e32 v[48:49], v[4:5]
	v_mov_b64_e32 v[52:53], v[4:5]
	v_mov_b64_e32 v[56:57], v[4:5]
	v_mov_b64_e32 v[60:61], v[4:5]
	v_mov_b64_e32 v[64:65], v[4:5]
	s_mov_b32 s77, 0
	v_mov_b32_e32 v69, v68
	v_mov_b32_e32 v70, v68
	v_mov_b32_e32 v71, v68
	v_mov_b32_e32 v72, v68
	v_mov_b32_e32 v73, v68
	v_mov_b32_e32 v74, v68
	v_mov_b32_e32 v75, v68
	v_mov_b32_e32 v76, v68
	v_mov_b32_e32 v77, v68
	v_mov_b32_e32 v78, v68
	v_mov_b32_e32 v79, v68
	v_mov_b32_e32 v80, v68
	v_mov_b32_e32 v81, v68
	v_mov_b32_e32 v82, v68
	v_mov_b32_e32 v83, v68
	v_mov_b32_e32 v88, v68
	v_mov_b32_e32 v89, v68
	v_mov_b32_e32 v90, v68
	v_mov_b32_e32 v91, v68
	v_mov_b32_e32 v92, v68
	v_mov_b32_e32 v93, v68
	v_mov_b32_e32 v94, v68
	v_mov_b32_e32 v95, v68
	v_mov_b32_e32 v96, v68
	v_mov_b32_e32 v97, v68
	v_mov_b32_e32 v98, v68
	v_mov_b32_e32 v99, v68
	v_mov_b32_e32 v100, v68
	v_mov_b32_e32 v101, v68
	v_mov_b32_e32 v102, v68
	v_mov_b32_e32 v103, v68
	v_mov_b32_e32 v104, v68
	v_mov_b32_e32 v105, v68
	v_mov_b32_e32 v106, v68
	v_mov_b32_e32 v107, v68
	v_mov_b32_e32 v108, v68
	v_mov_b32_e32 v109, v68
	v_mov_b32_e32 v110, v68
	v_mov_b32_e32 v111, v68
	v_mov_b32_e32 v112, v68
	v_mov_b32_e32 v113, v68
	v_mov_b32_e32 v114, v68
	v_mov_b32_e32 v115, v68
	v_mov_b32_e32 v116, v68
	v_mov_b32_e32 v117, v68
	v_mov_b32_e32 v118, v68
	v_mov_b32_e32 v119, v68
	v_mov_b32_e32 v120, v68
	v_mov_b32_e32 v121, v68
	v_mov_b32_e32 v122, v68
	v_mov_b32_e32 v123, v68
	v_mov_b32_e32 v124, v68
	v_mov_b32_e32 v125, v68
	v_mov_b32_e32 v126, v68
	v_mov_b32_e32 v127, v68
	v_mov_b32_e32 v128, v68
	v_mov_b32_e32 v129, v68
	v_mov_b32_e32 v130, v68
	v_mov_b32_e32 v131, v68
	v_mov_b32_e32 v132, v68
	v_mov_b32_e32 v133, v68
	v_mov_b32_e32 v134, v68
	v_mov_b32_e32 v135, v68
	s_barrier
	s_branch .LBB0_1154

.LBB0_1296:
	v_and_b32_e32 v4, 15, v6
	v_lshrrev_b32_e32 v5, 1, v6
	v_lshl_or_b32 v220, s4, 6, v4
	v_and_b32_e32 v7, 24, v5
	v_lshlrev_b32_e32 v5, 1, v7
	v_lshlrev_b32_e32 v8, 2, v220
	v_lshl_or_b32 v4, v4, 6, v5
	s_lshl_b32 s2, s4, 13
	v_and_b32_e32 v5, 32, v8
	v_bitop3_b32 v9, v4, s2, v5 bitop3:0xde
	s_lshl_b32 s2, s5, 5
	s_and_b32 s4, s2, 0x60
	v_lshlrev_b32_e32 v5, 2, v6
	s_lshl_b32 s2, s4, 7
	v_and_b32_e32 v5, 32, v5
	v_bitop3_b32 v10, v4, s2, v5 bitop3:0xde
	s_add_u32 s2, s14, 0x8000
	v_mov_b32_e32 v209, v3
	s_addc_u32 s3, s15, 0
	s_add_i32 s72, s11, 0x18000
	v_mov_b32_e32 v211, v3
	v_lshl_add_u64 v[4:5], s[2:3], 0, v[208:209]
	s_mov_b32 m0, s72
	global_load_lds_dwordx4 v[4:5], off
	v_lshl_add_u64 v[4:5], s[2:3], 0, v[210:211]
	s_add_i32 s73, s11, 0x1a000
	v_readlane_b32 s2, v254, 25
	s_mov_b32 m0, s73
	v_readlane_b32 s3, v254, 26
	s_add_i32 s74, s11, 0x8000
	v_mov_b32_e32 v213, v3
	global_load_lds_dwordx4 v[4:5], off
	v_lshl_add_u64 v[4:5], s[2:3], 0, v[2:3]
	s_mov_b32 m0, s74
	s_add_i32 s75, s11, 0xa000
	global_load_lds_dwordx4 v[4:5], off
	v_lshl_add_u64 v[4:5], s[2:3], 0, v[212:213]
	s_add_u32 s2, s14, 0xc000
	s_mov_b32 m0, s75
	s_addc_u32 s3, s15, 0
	s_add_i32 s76, s11, 0x1c000
	global_load_lds_dwordx4 v[4:5], off
	v_lshl_add_u64 v[4:5], s[2:3], 0, v[208:209]
	s_mov_b32 m0, s76
	s_add_i32 s77, s11, 0x1e000
	global_load_lds_dwordx4 v[4:5], off
	v_lshl_add_u64 v[4:5], s[2:3], 0, v[210:211]
	s_mov_b32 m0, s77
	s_cmpk_lt_u32 s38, 0x100
	global_load_lds_dwordx4 v[4:5], off
	s_waitcnt vmcnt(8)
	s_barrier
	s_waitcnt vmcnt(6)
	s_cselect_b64 s[38:39], -1, 0
	v_or_b32_e32 v239, s4, v7
	s_add_i32 s2, 0, 0x20000
	v_mov_b32_e32 v6, v3
	v_mov_b32_e32 v7, v3
	v_add_u32_e32 v240, s2, v8
	v_mov_b32_e32 v4, v3
	v_mov_b32_e32 v5, v3
	v_mov_b32_e32 v68, 0
	v_add_u32_e32 v241, 0, v10
	v_add_u32_e32 v242, 0, v9
	v_mov_b64_e32 v[10:11], v[6:7]
	v_mov_b64_e32 v[14:15], v[6:7]
	v_mov_b64_e32 v[18:19], v[6:7]
	v_mov_b64_e32 v[22:23], v[6:7]
	v_mov_b64_e32 v[26:27], v[6:7]
	v_mov_b64_e32 v[30:31], v[6:7]
	v_mov_b64_e32 v[34:35], v[6:7]
	v_mov_b64_e32 v[38:39], v[6:7]
	v_mov_b64_e32 v[42:43], v[6:7]
	v_mov_b64_e32 v[46:47], v[6:7]
	v_mov_b64_e32 v[50:51], v[6:7]
	v_mov_b64_e32 v[54:55], v[6:7]
	v_mov_b64_e32 v[58:59], v[6:7]
	v_mov_b64_e32 v[62:63], v[6:7]
	v_mov_b64_e32 v[66:67], v[6:7]
	v_or_b32_e32 v221, 16, v220
	v_or_b32_e32 v222, 32, v220
	v_or_b32_e32 v223, 48, v220
	v_add_u32_e32 v224, 0x80, v220
	v_add_u32_e32 v225, 0x90, v220
	v_add_u32_e32 v226, 0xa0, v220
	v_add_u32_e32 v227, 0xb0, v220
	s_mov_b32 s78, 0
	v_mov_b64_e32 v[8:9], v[4:5]
	v_mov_b64_e32 v[12:13], v[4:5]
	v_mov_b64_e32 v[16:17], v[4:5]
	v_mov_b64_e32 v[20:21], v[4:5]
	v_mov_b64_e32 v[24:25], v[4:5]
	v_mov_b64_e32 v[28:29], v[4:5]
	v_mov_b64_e32 v[32:33], v[4:5]
	v_mov_b64_e32 v[36:37], v[4:5]
	v_mov_b64_e32 v[40:41], v[4:5]
	v_mov_b64_e32 v[44:45], v[4:5]
	v_mov_b64_e32 v[48:49], v[4:5]
	v_mov_b64_e32 v[52:53], v[4:5]
	v_mov_b64_e32 v[56:57], v[4:5]
	v_mov_b64_e32 v[60:61], v[4:5]
	v_mov_b64_e32 v[64:65], v[4:5]
	s_mov_b32 s80, 0
	v_mov_b32_e32 v69, v68
	v_mov_b32_e32 v70, v68
	v_mov_b32_e32 v71, v68
	v_mov_b32_e32 v72, v68
	v_mov_b32_e32 v73, v68
	v_mov_b32_e32 v74, v68
	v_mov_b32_e32 v75, v68
	v_mov_b32_e32 v76, v68
	v_mov_b32_e32 v77, v68
	v_mov_b32_e32 v78, v68
	v_mov_b32_e32 v79, v68
	v_mov_b32_e32 v80, v68
	v_mov_b32_e32 v81, v68
	v_mov_b32_e32 v82, v68
	v_mov_b32_e32 v83, v68
	v_mov_b32_e32 v88, v68
	v_mov_b32_e32 v89, v68
	v_mov_b32_e32 v90, v68
	v_mov_b32_e32 v91, v68
	v_mov_b32_e32 v92, v68
	v_mov_b32_e32 v93, v68
	v_mov_b32_e32 v94, v68
	v_mov_b32_e32 v95, v68
	v_mov_b32_e32 v96, v68
	v_mov_b32_e32 v97, v68
	v_mov_b32_e32 v98, v68
	v_mov_b32_e32 v99, v68
	v_mov_b32_e32 v100, v68
	v_mov_b32_e32 v101, v68
	v_mov_b32_e32 v102, v68
	v_mov_b32_e32 v103, v68
	v_mov_b32_e32 v104, v68
	v_mov_b32_e32 v105, v68
	v_mov_b32_e32 v106, v68
	v_mov_b32_e32 v107, v68
	v_mov_b32_e32 v108, v68
	v_mov_b32_e32 v109, v68
	v_mov_b32_e32 v110, v68
	v_mov_b32_e32 v111, v68
	v_mov_b32_e32 v112, v68
	v_mov_b32_e32 v113, v68
	v_mov_b32_e32 v114, v68
	v_mov_b32_e32 v115, v68
	v_mov_b32_e32 v116, v68
	v_mov_b32_e32 v117, v68
	v_mov_b32_e32 v118, v68
	v_mov_b32_e32 v119, v68
	v_mov_b32_e32 v120, v68
	v_mov_b32_e32 v121, v68
	v_mov_b32_e32 v122, v68
	v_mov_b32_e32 v123, v68
	v_mov_b32_e32 v124, v68
	v_mov_b32_e32 v125, v68
	v_mov_b32_e32 v126, v68
	v_mov_b32_e32 v127, v68
	v_mov_b32_e32 v128, v68
	v_mov_b32_e32 v129, v68
	v_mov_b32_e32 v130, v68
	v_mov_b32_e32 v131, v68
	v_mov_b32_e32 v132, v68
	v_mov_b32_e32 v133, v68
	v_mov_b32_e32 v134, v68
	v_mov_b32_e32 v135, v68
	s_barrier
	s_branch .LBB0_1299

.LBB0_1412:
	v_and_b32_e32 v4, 15, v6
	v_lshrrev_b32_e32 v5, 1, v6
	v_lshl_or_b32 v220, s4, 6, v4
	v_and_b32_e32 v7, 24, v5
	v_lshlrev_b32_e32 v5, 1, v7
	v_lshlrev_b32_e32 v8, 2, v220
	v_lshl_or_b32 v4, v4, 6, v5
	s_lshl_b32 s2, s4, 13
	v_and_b32_e32 v5, 32, v8
	v_bitop3_b32 v9, v4, s2, v5 bitop3:0xde
	s_lshl_b32 s2, s5, 5
	s_and_b32 s4, s2, 0x60
	v_lshlrev_b32_e32 v5, 2, v6
	s_lshl_b32 s2, s4, 7
	v_and_b32_e32 v5, 32, v5
	v_bitop3_b32 v10, v4, s2, v5 bitop3:0xde
	s_add_u32 s2, s10, 0x8000
	v_mov_b32_e32 v209, v3
	s_addc_u32 s3, s11, 0
	s_add_i32 s63, s7, 0x18000
	v_mov_b32_e32 v211, v3
	v_lshl_add_u64 v[4:5], s[2:3], 0, v[208:209]
	s_mov_b32 m0, s63
	global_load_lds_dwordx4 v[4:5], off
	v_lshl_add_u64 v[4:5], s[2:3], 0, v[210:211]
	s_add_i32 s64, s7, 0x1a000
	v_readlane_b32 s2, v254, 25
	s_mov_b32 m0, s64
	v_readlane_b32 s3, v254, 26
	s_add_i32 s65, s7, 0x8000
	v_mov_b32_e32 v213, v3
	global_load_lds_dwordx4 v[4:5], off
	v_lshl_add_u64 v[4:5], s[2:3], 0, v[2:3]
	s_mov_b32 m0, s65
	s_add_i32 s66, s7, 0xa000
	global_load_lds_dwordx4 v[4:5], off
	v_lshl_add_u64 v[4:5], s[2:3], 0, v[212:213]
	s_add_u32 s2, s10, 0xc000
	s_mov_b32 m0, s66
	s_addc_u32 s3, s11, 0
	s_add_i32 s67, s7, 0x1c000
	global_load_lds_dwordx4 v[4:5], off
	v_lshl_add_u64 v[4:5], s[2:3], 0, v[208:209]
	s_mov_b32 m0, s67
	s_add_i32 s68, s7, 0x1e000
	global_load_lds_dwordx4 v[4:5], off
	v_lshl_add_u64 v[4:5], s[2:3], 0, v[210:211]
	s_mov_b32 m0, s68
	s_cmpk_lt_u32 s12, 0x100
	global_load_lds_dwordx4 v[4:5], off
	s_waitcnt vmcnt(8)
	s_barrier
	s_waitcnt vmcnt(6)
	s_cselect_b64 s[12:13], -1, 0
	v_or_b32_e32 v239, s4, v7
	s_add_i32 s2, 0, 0x20000
	v_mov_b32_e32 v6, v3
	v_mov_b32_e32 v7, v3
	v_add_u32_e32 v240, s2, v8
	v_mov_b32_e32 v4, v3
	v_mov_b32_e32 v5, v3
	v_mov_b32_e32 v68, 0
	v_add_u32_e32 v241, 0, v10
	v_add_u32_e32 v242, 0, v9
	v_mov_b64_e32 v[10:11], v[6:7]
	v_mov_b64_e32 v[14:15], v[6:7]
	v_mov_b64_e32 v[18:19], v[6:7]
	v_mov_b64_e32 v[22:23], v[6:7]
	v_mov_b64_e32 v[26:27], v[6:7]
	v_mov_b64_e32 v[30:31], v[6:7]
	v_mov_b64_e32 v[34:35], v[6:7]
	v_mov_b64_e32 v[38:39], v[6:7]
	v_mov_b64_e32 v[42:43], v[6:7]
	v_mov_b64_e32 v[46:47], v[6:7]
	v_mov_b64_e32 v[50:51], v[6:7]
	v_mov_b64_e32 v[54:55], v[6:7]
	v_mov_b64_e32 v[58:59], v[6:7]
	v_mov_b64_e32 v[62:63], v[6:7]
	v_mov_b64_e32 v[66:67], v[6:7]
	v_or_b32_e32 v221, 16, v220
	v_or_b32_e32 v222, 32, v220
	v_or_b32_e32 v223, 48, v220
	v_add_u32_e32 v224, 0x80, v220
	v_add_u32_e32 v225, 0x90, v220
	v_add_u32_e32 v226, 0xa0, v220
	v_add_u32_e32 v227, 0xb0, v220
	s_mov_b32 s69, 0
	v_mov_b64_e32 v[8:9], v[4:5]
	v_mov_b64_e32 v[12:13], v[4:5]
	v_mov_b64_e32 v[16:17], v[4:5]
	v_mov_b64_e32 v[20:21], v[4:5]
	v_mov_b64_e32 v[24:25], v[4:5]
	v_mov_b64_e32 v[28:29], v[4:5]
	v_mov_b64_e32 v[32:33], v[4:5]
	v_mov_b64_e32 v[36:37], v[4:5]
	v_mov_b64_e32 v[40:41], v[4:5]
	v_mov_b64_e32 v[44:45], v[4:5]
	v_mov_b64_e32 v[48:49], v[4:5]
	v_mov_b64_e32 v[52:53], v[4:5]
	v_mov_b64_e32 v[56:57], v[4:5]
	v_mov_b64_e32 v[60:61], v[4:5]
	v_mov_b64_e32 v[64:65], v[4:5]
	s_mov_b32 s71, 0
	v_mov_b32_e32 v69, v68
	v_mov_b32_e32 v70, v68
	v_mov_b32_e32 v71, v68
	v_mov_b32_e32 v72, v68
	v_mov_b32_e32 v73, v68
	v_mov_b32_e32 v74, v68
	v_mov_b32_e32 v75, v68
	v_mov_b32_e32 v76, v68
	v_mov_b32_e32 v77, v68
	v_mov_b32_e32 v78, v68
	v_mov_b32_e32 v79, v68
	v_mov_b32_e32 v80, v68
	v_mov_b32_e32 v81, v68
	v_mov_b32_e32 v82, v68
	v_mov_b32_e32 v83, v68
	v_mov_b32_e32 v88, v68
	v_mov_b32_e32 v89, v68
	v_mov_b32_e32 v90, v68
	v_mov_b32_e32 v91, v68
	v_mov_b32_e32 v92, v68
	v_mov_b32_e32 v93, v68
	v_mov_b32_e32 v94, v68
	v_mov_b32_e32 v95, v68
	v_mov_b32_e32 v96, v68
	v_mov_b32_e32 v97, v68
	v_mov_b32_e32 v98, v68
	v_mov_b32_e32 v99, v68
	v_mov_b32_e32 v100, v68
	v_mov_b32_e32 v101, v68
	v_mov_b32_e32 v102, v68
	v_mov_b32_e32 v103, v68
	v_mov_b32_e32 v104, v68
	v_mov_b32_e32 v105, v68
	v_mov_b32_e32 v106, v68
	v_mov_b32_e32 v107, v68
	v_mov_b32_e32 v108, v68
	v_mov_b32_e32 v109, v68
	v_mov_b32_e32 v110, v68
	v_mov_b32_e32 v111, v68
	v_mov_b32_e32 v112, v68
	v_mov_b32_e32 v113, v68
	v_mov_b32_e32 v114, v68
	v_mov_b32_e32 v115, v68
	v_mov_b32_e32 v116, v68
	v_mov_b32_e32 v117, v68
	v_mov_b32_e32 v118, v68
	v_mov_b32_e32 v119, v68
	v_mov_b32_e32 v120, v68
	v_mov_b32_e32 v121, v68
	v_mov_b32_e32 v122, v68
	v_mov_b32_e32 v123, v68
	v_mov_b32_e32 v124, v68
	v_mov_b32_e32 v125, v68
	v_mov_b32_e32 v126, v68
	v_mov_b32_e32 v127, v68
	v_mov_b32_e32 v128, v68
	v_mov_b32_e32 v129, v68
	v_mov_b32_e32 v130, v68
	v_mov_b32_e32 v131, v68
	v_mov_b32_e32 v132, v68
	v_mov_b32_e32 v133, v68
	v_mov_b32_e32 v134, v68
	v_mov_b32_e32 v135, v68
	s_barrier
	s_branch .LBB0_1415
